# baseline (speedup 1.0000x reference)
.Lp1_loop:
	s_waitcnt vmcnt(4)
	ds_write_b128 v88, v[146:149]
	ds_write_b128 v89, v[150:153]
	ds_write_b128 v88, v[154:157] offset:9216
	ds_write_b128 v89, v[158:161] offset:9216
	global_load_dwordx4 v[112:115], v128, s[24:25]
	global_load_dwordx4 v[116:119], v86, s[24:25]
	s_add_u32 s24, s24, 0x2000
	s_addc_u32 s25, s25, 0
	global_load_dwordx4 v[120:123], v128, s[24:25]
	global_load_dwordx4 v[124:127], v86, s[24:25]
	s_add_u32 s24, s24, 0x2000
	s_addc_u32 s25, s25, 0
	global_store_dwordx4 v90, v[92:95], s[30:31]
	global_store_dwordx4 v90, v[92:95], s[30:31] offset:1024
	s_add_u32 s30, s30, 0x2000
	s_addc_u32 s31, s31, 0
	global_store_dwordx4 v90, v[92:95], s[30:31]
	global_store_dwordx4 v90, v[92:95], s[30:31] offset:1024
	s_add_u32 s30, s30, 0x2000
	s_addc_u32 s31, s31, 0
	ds_read_b128 v[168:171], v167
	ds_read_b128 v[172:175], v167 offset:4608
	ds_read_b128 v[176:179], v167 offset:32
	ds_read_b128 v[180:183], v167 offset:4640
	ds_read_b128 v[184:187], v167 offset:64
	ds_read_b128 v[188:191], v167 offset:4672
	ds_read_b128 v[192:195], v167 offset:96
	ds_read_b128 v[196:199], v167 offset:4704
	v_mov_b32_e32 v200, 0
	v_mov_b32_e32 v201, 0
	v_mov_b32_e32 v202, 0
	v_mov_b32_e32 v83, 0
	v_exp_f32_e32 v34, v34
	v_exp_f32_e32 v35, v35
	v_add_f32_e32 v200, v200, v34
	v_exp_f32_e32 v36, v36
	v_add_f32_e32 v201, v201, v35
	v_exp_f32_e32 v37, v37
	s_waitcnt lgkmcnt(7)
	v_mfma_f32_32x32x16_f16 v[2:17], v[168:171], v[108:111], v[130:145]
	v_add_f32_e32 v202, v202, v36
	v_exp_f32_e32 v38, v38
	v_add_f32_e32 v83, v83, v37
	v_exp_f32_e32 v39, v39
	v_add_f32_e32 v200, v200, v38
	v_exp_f32_e32 v40, v40
	s_waitcnt lgkmcnt(6)
	v_mfma_f32_32x32x16_f16 v[18:33], v[172:175], v[108:111], v[130:145]
	v_add_f32_e32 v201, v201, v39
	v_exp_f32_e32 v41, v41
	v_add_f32_e32 v202, v202, v40
	v_exp_f32_e32 v42, v42
	v_add_f32_e32 v83, v83, v41
	v_exp_f32_e32 v43, v43
	s_waitcnt lgkmcnt(5)
	v_mfma_f32_32x32x16_f16 v[2:17], v[176:179], v[104:107], v[2:17]
	v_add_f32_e32 v200, v200, v42
	v_exp_f32_e32 v44, v44
	v_add_f32_e32 v201, v201, v43
	v_exp_f32_e32 v45, v45
	v_add_f32_e32 v202, v202, v44
	v_exp_f32_e32 v46, v46
	s_waitcnt lgkmcnt(4)
	v_mfma_f32_32x32x16_f16 v[18:33], v[180:183], v[104:107], v[18:33]
	v_add_f32_e32 v83, v83, v45
	v_exp_f32_e32 v47, v47
	v_add_f32_e32 v200, v200, v46
	v_exp_f32_e32 v48, v48
	v_add_f32_e32 v201, v201, v47
	v_exp_f32_e32 v49, v49
	s_waitcnt lgkmcnt(3)
	v_mfma_f32_32x32x16_f16 v[2:17], v[184:187], v[100:103], v[2:17]
	v_add_f32_e32 v202, v202, v48
	v_exp_f32_e32 v50, v50
	v_add_f32_e32 v83, v83, v49
	v_exp_f32_e32 v51, v51
	v_add_f32_e32 v200, v200, v50
	v_exp_f32_e32 v52, v52
	s_waitcnt lgkmcnt(2)
	v_mfma_f32_32x32x16_f16 v[18:33], v[188:191], v[100:103], v[18:33]
	v_add_f32_e32 v201, v201, v51
	v_exp_f32_e32 v53, v53
	v_add_f32_e32 v202, v202, v52
	v_exp_f32_e32 v54, v54
	v_add_f32_e32 v83, v83, v53
	v_exp_f32_e32 v55, v55
	s_waitcnt lgkmcnt(1)
	v_mfma_f32_32x32x16_f16 v[2:17], v[192:195], v[96:99], v[2:17]
	v_add_f32_e32 v200, v200, v54
	v_exp_f32_e32 v56, v56
	v_add_f32_e32 v201, v201, v55
	v_exp_f32_e32 v57, v57
	v_add_f32_e32 v202, v202, v56
	v_exp_f32_e32 v58, v58
	s_waitcnt lgkmcnt(0)
	v_mfma_f32_32x32x16_f16 v[18:33], v[196:199], v[96:99], v[18:33]
	ds_read_b128 v[204:207], v167 offset:9216
	ds_read_b128 v[208:211], v167 offset:13824
	ds_read_b128 v[212:215], v167 offset:9248
	ds_read_b128 v[216:219], v167 offset:13856
	ds_read_b128 v[220:223], v167 offset:9280
	ds_read_b128 v[224:227], v167 offset:13888
	ds_read_b128 v[228:231], v167 offset:9312
	ds_read_b128 v[232:235], v167 offset:13920
	v_add_f32_e32 v83, v83, v57
	v_exp_f32_e32 v59, v59
	v_add_f32_e32 v200, v200, v58
	v_exp_f32_e32 v60, v60
	v_add_f32_e32 v201, v201, v59
	v_exp_f32_e32 v61, v61
	v_add_f32_e32 v202, v202, v60
	v_exp_f32_e32 v62, v62
	v_add_f32_e32 v83, v83, v61
	v_exp_f32_e32 v63, v63
	v_add_f32_e32 v200, v200, v62
	v_exp_f32_e32 v64, v64
	v_add_f32_e32 v201, v201, v63
	v_exp_f32_e32 v65, v65
	v_add_f32_e32 v202, v202, v64
	v_add_f32_e32 v83, v83, v65
	v_add_f32_e32 v200, v200, v201
	v_add_f32_e32 v202, v202, v83
	v_add_f32_e32 v200, v200, v202
	v_add_f32_e32 v82, v82, v200
	v_max3_f32 v84, v2, v3, v4
	v_max3_f32 v85, v18, v19, v20
	v_max3_f32 v84, v84, v5, v6
	v_max3_f32 v85, v85, v21, v22
	v_max3_f32 v84, v84, v7, v8
	v_max3_f32 v85, v85, v23, v24
	v_max3_f32 v84, v84, v9, v10
	v_max3_f32 v85, v85, v25, v26
	v_max3_f32 v84, v84, v11, v12
	v_max3_f32 v85, v85, v27, v28
	v_max3_f32 v84, v84, v13, v14
	v_max3_f32 v85, v85, v29, v30
	v_max3_f32 v84, v84, v15, v16
	v_max3_f32 v85, v85, v31, v32
	v_max3_f32 v84, v84, v17, v33
	s_nop 0
	v_max_f32_e32 v84, v84, v85
	s_nop 0
	v_cmp_lt_f32_e32 vcc, s11, v84
	s_cbranch_vccnz .Lp1_rare_d0a

.Lp1_back_d0b:
	s_waitcnt lgkmcnt(0)
	s_barrier
	s_waitcnt vmcnt(4)
	ds_write_b128 v77, v[112:115]
	ds_write_b128 v78, v[116:119]
	ds_write_b128 v77, v[120:123] offset:9216
	ds_write_b128 v78, v[124:127] offset:9216
	global_load_dwordx4 v[146:149], v128, s[24:25]
	global_load_dwordx4 v[150:153], v86, s[24:25]
	s_add_u32 s24, s24, 0x2000
	s_addc_u32 s25, s25, 0
	global_load_dwordx4 v[154:157], v128, s[24:25]
	global_load_dwordx4 v[158:161], v86, s[24:25]
	s_add_u32 s24, s24, 0x2000
	s_addc_u32 s25, s25, 0
	global_store_dwordx4 v90, v[92:95], s[30:31]
	global_store_dwordx4 v90, v[92:95], s[30:31] offset:1024
	s_add_u32 s30, s30, 0x2000
	s_addc_u32 s31, s31, 0
	global_store_dwordx4 v90, v[92:95], s[30:31]
	global_store_dwordx4 v90, v[92:95], s[30:31] offset:1024
	s_add_u32 s30, s30, 0x2000
	s_addc_u32 s31, s31, 0
	ds_read_b128 v[168:171], v87
	ds_read_b128 v[172:175], v87 offset:4608
	ds_read_b128 v[176:179], v87 offset:32
	ds_read_b128 v[180:183], v87 offset:4640
	ds_read_b128 v[184:187], v87 offset:64
	ds_read_b128 v[188:191], v87 offset:4672
	ds_read_b128 v[192:195], v87 offset:96
	ds_read_b128 v[196:199], v87 offset:4704
	v_mov_b32_e32 v200, 0
	v_mov_b32_e32 v201, 0
	v_mov_b32_e32 v202, 0
	v_mov_b32_e32 v83, 0
	v_exp_f32_e32 v34, v34
	v_exp_f32_e32 v35, v35
	v_add_f32_e32 v200, v200, v34
	v_exp_f32_e32 v36, v36
	v_add_f32_e32 v201, v201, v35
	v_exp_f32_e32 v37, v37
	s_waitcnt lgkmcnt(7)
	v_mfma_f32_32x32x16_f16 v[2:17], v[168:171], v[108:111], v[130:145]
	v_add_f32_e32 v202, v202, v36
	v_exp_f32_e32 v38, v38
	v_add_f32_e32 v83, v83, v37
	v_exp_f32_e32 v39, v39
	v_add_f32_e32 v200, v200, v38
	v_exp_f32_e32 v40, v40
	s_waitcnt lgkmcnt(6)
	v_mfma_f32_32x32x16_f16 v[18:33], v[172:175], v[108:111], v[130:145]
	v_add_f32_e32 v201, v201, v39
	v_exp_f32_e32 v41, v41
	v_add_f32_e32 v202, v202, v40
	v_exp_f32_e32 v42, v42
	v_add_f32_e32 v83, v83, v41
	v_exp_f32_e32 v43, v43
	s_waitcnt lgkmcnt(5)
	v_mfma_f32_32x32x16_f16 v[2:17], v[176:179], v[104:107], v[2:17]
	v_add_f32_e32 v200, v200, v42
	v_exp_f32_e32 v44, v44
	v_add_f32_e32 v201, v201, v43
	v_exp_f32_e32 v45, v45
	v_add_f32_e32 v202, v202, v44
	v_exp_f32_e32 v46, v46
	s_waitcnt lgkmcnt(4)
	v_mfma_f32_32x32x16_f16 v[18:33], v[180:183], v[104:107], v[18:33]
	v_add_f32_e32 v83, v83, v45
	v_exp_f32_e32 v47, v47
	v_add_f32_e32 v200, v200, v46
	v_exp_f32_e32 v48, v48
	v_add_f32_e32 v201, v201, v47
	v_exp_f32_e32 v49, v49
	s_waitcnt lgkmcnt(3)
	v_mfma_f32_32x32x16_f16 v[2:17], v[184:187], v[100:103], v[2:17]
	v_add_f32_e32 v202, v202, v48
	v_exp_f32_e32 v50, v50
	v_add_f32_e32 v83, v83, v49
	v_exp_f32_e32 v51, v51
	v_add_f32_e32 v200, v200, v50
	v_exp_f32_e32 v52, v52
	s_waitcnt lgkmcnt(2)
	v_mfma_f32_32x32x16_f16 v[18:33], v[188:191], v[100:103], v[18:33]
	v_add_f32_e32 v201, v201, v51
	v_exp_f32_e32 v53, v53
	v_add_f32_e32 v202, v202, v52
	v_exp_f32_e32 v54, v54
	v_add_f32_e32 v83, v83, v53
	v_exp_f32_e32 v55, v55
	s_waitcnt lgkmcnt(1)
	v_mfma_f32_32x32x16_f16 v[2:17], v[192:195], v[96:99], v[2:17]
	v_add_f32_e32 v200, v200, v54
	v_exp_f32_e32 v56, v56
	v_add_f32_e32 v201, v201, v55
	v_exp_f32_e32 v57, v57
	v_add_f32_e32 v202, v202, v56
	v_exp_f32_e32 v58, v58
	s_waitcnt lgkmcnt(0)
	v_mfma_f32_32x32x16_f16 v[18:33], v[196:199], v[96:99], v[18:33]
	ds_read_b128 v[204:207], v87 offset:9216
	ds_read_b128 v[208:211], v87 offset:13824
	ds_read_b128 v[212:215], v87 offset:9248
	ds_read_b128 v[216:219], v87 offset:13856
	ds_read_b128 v[220:223], v87 offset:9280
	ds_read_b128 v[224:227], v87 offset:13888
	ds_read_b128 v[228:231], v87 offset:9312
	ds_read_b128 v[232:235], v87 offset:13920
	v_add_f32_e32 v83, v83, v57
	v_exp_f32_e32 v59, v59
	v_add_f32_e32 v200, v200, v58
	v_exp_f32_e32 v60, v60
	v_add_f32_e32 v201, v201, v59
	v_exp_f32_e32 v61, v61
	v_add_f32_e32 v202, v202, v60
	v_exp_f32_e32 v62, v62
	v_add_f32_e32 v83, v83, v61
	v_exp_f32_e32 v63, v63
	v_add_f32_e32 v200, v200, v62
	v_exp_f32_e32 v64, v64
	v_add_f32_e32 v201, v201, v63
	v_exp_f32_e32 v65, v65
	v_add_f32_e32 v202, v202, v64
	v_add_f32_e32 v83, v83, v65
	v_add_f32_e32 v200, v200, v201
	v_add_f32_e32 v202, v202, v83
	v_add_f32_e32 v200, v200, v202
	v_add_f32_e32 v82, v82, v200
	v_max3_f32 v84, v2, v3, v4
	v_max3_f32 v85, v18, v19, v20
	v_max3_f32 v84, v84, v5, v6
	v_max3_f32 v85, v85, v21, v22
	v_max3_f32 v84, v84, v7, v8
	v_max3_f32 v85, v85, v23, v24
	v_max3_f32 v84, v84, v9, v10
	v_max3_f32 v85, v85, v25, v26
	v_max3_f32 v84, v84, v11, v12
	v_max3_f32 v85, v85, v27, v28
	v_max3_f32 v84, v84, v13, v14
	v_max3_f32 v85, v85, v29, v30
	v_max3_f32 v84, v84, v15, v16
	v_max3_f32 v85, v85, v31, v32
	v_max3_f32 v84, v84, v17, v33
	s_nop 0
	v_max_f32_e32 v84, v84, v85
	s_nop 0
	v_cmp_lt_f32_e32 vcc, s11, v84
	s_cbranch_vccnz .Lp1_rare_d1a
